# prologue: XN rows 8-deep in flight (fast path), two spurious vmcnt(0) removed from the pipelined weight-tile loads
# baseline (speedup 1.0000x reference)
.LBB0_936:
	v_add_u32_e32 v54, 54, v40
	v_ashrrev_i32_e32 v106, 31, v54
	v_mad_u64_u32 v[54:55], s[16:17], v54, s6, 0
	v_mov_b32_e32 v56, v55
	v_mad_u64_u32 v[106:107], s[16:17], v106, s6, v[56:57]
	v_mov_b32_e32 v55, v106
	v_lshl_add_u64 v[54:55], v[54:55], 2, v[38:39]
	global_load_dword v106, v[54:55], off nt
	v_mov_b32_e32 v55, 1.0
	s_and_b64 vcc, exec, s[38:39]
	v_mov_b32_e32 v56, 1.0
	s_cbranch_vccnz .LBB0_938
	global_load_dword v56, v[42:43], off offset:224

.LBB0_940:
	v_add_u32_e32 v54, 58, v40
	v_mad_u64_u32 v[110:111], s[16:17], v54, s6, 0
	v_ashrrev_i32_e32 v107, 31, v54
	v_mov_b32_e32 v54, v111
	v_mad_u64_u32 v[112:113], s[16:17], v107, s6, v[54:55]
	v_mov_b32_e32 v111, v112
	v_lshl_add_u64 v[110:111], v[110:111], 2, v[38:39]
	global_load_dword v109, v[110:111], off nt
	v_mov_b32_e32 v107, 1.0
	s_and_b64 vcc, exec, s[38:39]
	v_mov_b32_e32 v54, 1.0
	s_cbranch_vccnz .LBB0_942
	global_load_dword v54, v[42:43], off offset:240

.LBB0_1051:
	s_cmpk_gt_i32 s4, 0x3fff
	s_cbranch_scc1 .LBB0_1062
	s_load_dwordx2 s[14:15], s[0:1], 0x0
	v_ashrrev_i32_e32 v195, 31, v194
	s_waitcnt lgkmcnt(0)
	v_lshl_add_u64 v[2:3], v[194:195], 3, s[26:27]
	s_add_u32 s6, s26, 0x30000000
	v_cmp_eq_u32_e32 vcc, 0, v194
	v_lshl_add_u64 v[34:35], v[194:195], 4, s[14:15]
	s_mov_b64 s[14:15], 0x1a000000
	v_cmp_ne_u32_e64 s[38:39], 0, v194
	v_lshl_add_u64 v[36:37], v[2:3], 0, s[14:15]
	s_addc_u32 s14, s27, 0
	s_mul_i32 s16, s88, 7
	s_add_i32 s16, s16, s4
	s_cmpk_gt_i32 s16, 0x3fff
	s_cbranch_scc1 .LBB0_1055
	s_mov_b32 s26, s4
	s_mov_b32 s27, 0
	s_lshl_b64 s[16:17], s[26:27], 12
	v_lshl_add_u64 v[118:119], v[34:35], 0, s[16:17]
	global_load_dwordx4 v[2:5], v[118:119], off nt
	global_load_dwordx4 v[6:9], v[118:119], off offset:1024 nt
	global_load_dwordx4 v[10:13], v[118:119], off offset:2048 nt
	global_load_dwordx4 v[14:17], v[118:119], off offset:3072 nt
	s_add_i32 s26, s26, s88
	s_lshl_b64 s[16:17], s[26:27], 12
	v_lshl_add_u64 v[118:119], v[34:35], 0, s[16:17]
	global_load_dwordx4 v[18:21], v[118:119], off nt
	global_load_dwordx4 v[22:25], v[118:119], off offset:1024 nt
	global_load_dwordx4 v[26:29], v[118:119], off offset:2048 nt
	global_load_dwordx4 v[30:33], v[118:119], off offset:3072 nt
	s_add_i32 s26, s26, s88
	s_lshl_b64 s[16:17], s[26:27], 12
	v_lshl_add_u64 v[118:119], v[34:35], 0, s[16:17]
	global_load_dwordx4 v[38:41], v[118:119], off nt
	global_load_dwordx4 v[42:45], v[118:119], off offset:1024 nt
	global_load_dwordx4 v[46:49], v[118:119], off offset:2048 nt
	global_load_dwordx4 v[50:53], v[118:119], off offset:3072 nt
	s_add_i32 s26, s26, s88
	s_lshl_b64 s[16:17], s[26:27], 12
	v_lshl_add_u64 v[118:119], v[34:35], 0, s[16:17]
	global_load_dwordx4 v[54:57], v[118:119], off nt
	global_load_dwordx4 v[58:61], v[118:119], off offset:1024 nt
	global_load_dwordx4 v[62:65], v[118:119], off offset:2048 nt
	global_load_dwordx4 v[66:69], v[118:119], off offset:3072 nt
	s_add_i32 s26, s26, s88
	s_lshl_b64 s[16:17], s[26:27], 12
	v_lshl_add_u64 v[118:119], v[34:35], 0, s[16:17]
	global_load_dwordx4 v[70:73], v[118:119], off nt
	global_load_dwordx4 v[74:77], v[118:119], off offset:1024 nt
	global_load_dwordx4 v[78:81], v[118:119], off offset:2048 nt
	global_load_dwordx4 v[82:85], v[118:119], off offset:3072 nt
	s_add_i32 s26, s26, s88
	s_lshl_b64 s[16:17], s[26:27], 12
	v_lshl_add_u64 v[118:119], v[34:35], 0, s[16:17]
	global_load_dwordx4 v[86:89], v[118:119], off nt
	global_load_dwordx4 v[90:93], v[118:119], off offset:1024 nt
	global_load_dwordx4 v[94:97], v[118:119], off offset:2048 nt
	global_load_dwordx4 v[98:101], v[118:119], off offset:3072 nt
	s_add_i32 s26, s26, s88
	s_lshl_b64 s[16:17], s[26:27], 12
	v_lshl_add_u64 v[118:119], v[34:35], 0, s[16:17]
	global_load_dwordx4 v[102:105], v[118:119], off nt
	global_load_dwordx4 v[106:109], v[118:119], off offset:1024 nt
	global_load_dwordx4 v[110:113], v[118:119], off offset:2048 nt
	global_load_dwordx4 v[114:117], v[118:119], off offset:3072 nt
	s_add_i32 s26, s26, s88
	s_mov_b32 s5, s26
	s_mov_b32 s26, s4
	s_waitcnt vmcnt(24)
	v_mul_f32_e32 v0, v2, v2
	v_mul_f32_e32 v118, v3, v3
	v_mul_f32_e32 v119, v4, v4
	v_mul_f32_e32 v120, v5, v5
	v_fmac_f32_e32 v0, v6, v6
	v_fmac_f32_e32 v118, v7, v7
	v_fmac_f32_e32 v119, v8, v8
	v_fmac_f32_e32 v120, v9, v9
	v_fmac_f32_e32 v0, v10, v10
	v_fmac_f32_e32 v118, v11, v11
	v_fmac_f32_e32 v119, v12, v12
	v_fmac_f32_e32 v120, v13, v13
	v_fmac_f32_e32 v0, v14, v14
	v_fmac_f32_e32 v118, v15, v15
	v_fmac_f32_e32 v119, v16, v16
	v_fmac_f32_e32 v120, v17, v17
	v_add_f32_e32 v0, v0, v118
	v_add_f32_e32 v119, v119, v120
	v_add_f32_e32 v0, v0, v119
	s_nop 1
	v_add_f32_dpp v0, v0, v0 quad_perm:[1,0,3,2] row_mask:0xf bank_mask:0xf bound_ctrl:1
	s_nop 1
	v_add_f32_dpp v0, v0, v0 quad_perm:[2,3,0,1] row_mask:0xf bank_mask:0xf bound_ctrl:1
	s_nop 1
	v_add_f32_dpp v0, v0, v0 row_half_mirror row_mask:0xf bank_mask:0xf bound_ctrl:1
	s_nop 1
	v_add_f32_dpp v0, v0, v0 row_mirror row_mask:0xf bank_mask:0xf bound_ctrl:1
	v_mov_b32_e32 v118, v0
	s_nop 1
	v_permlane16_swap_b32_e32 v0, v118
	v_add_f32_e32 v0, v0, v118
	v_mov_b32_e32 v118, v0
	s_nop 1
	v_permlane32_swap_b32_e32 v0, v118
	s_and_saveexec_b64 s[30:31], vcc
	v_add_f32_e32 v0, v0, v118
	v_fmamk_f32 v0, v0, 0x3a800000, v190
	v_mul_f32_e32 v118, 0x4b800000, v0
	v_cmp_gt_f32_e64 s[40:41], s96, v0
	s_lshl_b64 s[16:17], s[26:27], 2
	s_add_u32 s16, s6, s16
	v_cndmask_b32_e64 v0, v0, v118, s[40:41]
	v_rsq_f32_e32 v0, v0
	s_addc_u32 s17, s14, s17
	v_mul_f32_e32 v118, 0x45800000, v0
	v_cndmask_b32_e64 v0, v0, v118, s[40:41]
	global_store_dword v1, v0, s[16:17]
	s_or_b64 exec, exec, s[30:31]
	s_lshl_b64 s[16:17], s[26:27], 11
	v_cvt_pk_bf16_f32 v2, v2, v3
	v_cvt_pk_bf16_f32 v3, v4, v5
	v_cvt_pk_bf16_f32 v6, v6, v7
	v_cvt_pk_bf16_f32 v7, v8, v9
	v_cvt_pk_bf16_f32 v10, v10, v11
	v_cvt_pk_bf16_f32 v11, v12, v13
	v_cvt_pk_bf16_f32 v14, v14, v15
	v_cvt_pk_bf16_f32 v15, v16, v17
	v_lshl_add_u64 v[120:121], v[36:37], 0, s[16:17]
	global_store_dwordx2 v[120:121], v[2:3], off
	global_store_dwordx2 v[120:121], v[6:7], off offset:512
	global_store_dwordx2 v[120:121], v[10:11], off offset:1024
	global_store_dwordx2 v[120:121], v[14:15], off offset:1536
	s_mov_b32 s16, s5
	s_mov_b32 s17, 0
	s_lshl_b64 s[16:17], s[16:17], 12
	v_lshl_add_u64 v[118:119], v[34:35], 0, s[16:17]
	global_load_dwordx4 v[2:5], v[118:119], off nt
	global_load_dwordx4 v[6:9], v[118:119], off offset:1024 nt
	global_load_dwordx4 v[10:13], v[118:119], off offset:2048 nt
	global_load_dwordx4 v[14:17], v[118:119], off offset:3072 nt
	s_add_i32 s26, s26, s88
	s_waitcnt vmcnt(29)
	v_mul_f32_e32 v0, v18, v18
	v_mul_f32_e32 v118, v19, v19
	v_mul_f32_e32 v119, v20, v20
	v_mul_f32_e32 v120, v21, v21
	v_fmac_f32_e32 v0, v22, v22
	v_fmac_f32_e32 v118, v23, v23
	v_fmac_f32_e32 v119, v24, v24
	v_fmac_f32_e32 v120, v25, v25
	v_fmac_f32_e32 v0, v26, v26
	v_fmac_f32_e32 v118, v27, v27
	v_fmac_f32_e32 v119, v28, v28
	v_fmac_f32_e32 v120, v29, v29
	v_fmac_f32_e32 v0, v30, v30
	v_fmac_f32_e32 v118, v31, v31
	v_fmac_f32_e32 v119, v32, v32
	v_fmac_f32_e32 v120, v33, v33
	v_add_f32_e32 v0, v0, v118
	v_add_f32_e32 v119, v119, v120
	v_add_f32_e32 v0, v0, v119
	s_nop 1
	v_add_f32_dpp v0, v0, v0 quad_perm:[1,0,3,2] row_mask:0xf bank_mask:0xf bound_ctrl:1
	s_nop 1
	v_add_f32_dpp v0, v0, v0 quad_perm:[2,3,0,1] row_mask:0xf bank_mask:0xf bound_ctrl:1
	s_nop 1
	v_add_f32_dpp v0, v0, v0 row_half_mirror row_mask:0xf bank_mask:0xf bound_ctrl:1
	s_nop 1
	v_add_f32_dpp v0, v0, v0 row_mirror row_mask:0xf bank_mask:0xf bound_ctrl:1
	v_mov_b32_e32 v118, v0
	s_nop 1
	v_permlane16_swap_b32_e32 v0, v118
	v_add_f32_e32 v0, v0, v118
	v_mov_b32_e32 v118, v0
	s_nop 1
	v_permlane32_swap_b32_e32 v0, v118
	s_and_saveexec_b64 s[30:31], vcc
	v_add_f32_e32 v0, v0, v118
	v_fmamk_f32 v0, v0, 0x3a800000, v190
	v_mul_f32_e32 v118, 0x4b800000, v0
	v_cmp_gt_f32_e64 s[40:41], s96, v0
	s_lshl_b64 s[16:17], s[26:27], 2
	s_add_u32 s16, s6, s16
	v_cndmask_b32_e64 v0, v0, v118, s[40:41]
	v_rsq_f32_e32 v0, v0
	s_addc_u32 s17, s14, s17
	v_mul_f32_e32 v118, 0x45800000, v0
	v_cndmask_b32_e64 v0, v0, v118, s[40:41]
	global_store_dword v1, v0, s[16:17]
	s_or_b64 exec, exec, s[30:31]
	s_lshl_b64 s[16:17], s[26:27], 11
	v_cvt_pk_bf16_f32 v18, v18, v19
	v_cvt_pk_bf16_f32 v19, v20, v21
	v_cvt_pk_bf16_f32 v22, v22, v23
	v_cvt_pk_bf16_f32 v23, v24, v25
	v_cvt_pk_bf16_f32 v26, v26, v27
	v_cvt_pk_bf16_f32 v27, v28, v29
	v_cvt_pk_bf16_f32 v30, v30, v31
	v_cvt_pk_bf16_f32 v31, v32, v33
	v_lshl_add_u64 v[120:121], v[36:37], 0, s[16:17]
	global_store_dwordx2 v[120:121], v[18:19], off
	global_store_dwordx2 v[120:121], v[22:23], off offset:512
	global_store_dwordx2 v[120:121], v[26:27], off offset:1024
	global_store_dwordx2 v[120:121], v[30:31], off offset:1536
	s_add_i32 s26, s26, s88
	s_waitcnt vmcnt(30)
	v_mul_f32_e32 v0, v38, v38
	v_mul_f32_e32 v118, v39, v39
	v_mul_f32_e32 v119, v40, v40
	v_mul_f32_e32 v120, v41, v41
	v_fmac_f32_e32 v0, v42, v42
	v_fmac_f32_e32 v118, v43, v43
	v_fmac_f32_e32 v119, v44, v44
	v_fmac_f32_e32 v120, v45, v45
	v_fmac_f32_e32 v0, v46, v46
	v_fmac_f32_e32 v118, v47, v47
	v_fmac_f32_e32 v119, v48, v48
	v_fmac_f32_e32 v120, v49, v49
	v_fmac_f32_e32 v0, v50, v50
	v_fmac_f32_e32 v118, v51, v51
	v_fmac_f32_e32 v119, v52, v52
	v_fmac_f32_e32 v120, v53, v53
	v_add_f32_e32 v0, v0, v118
	v_add_f32_e32 v119, v119, v120
	v_add_f32_e32 v0, v0, v119
	s_nop 1
	v_add_f32_dpp v0, v0, v0 quad_perm:[1,0,3,2] row_mask:0xf bank_mask:0xf bound_ctrl:1
	s_nop 1
	v_add_f32_dpp v0, v0, v0 quad_perm:[2,3,0,1] row_mask:0xf bank_mask:0xf bound_ctrl:1
	s_nop 1
	v_add_f32_dpp v0, v0, v0 row_half_mirror row_mask:0xf bank_mask:0xf bound_ctrl:1
	s_nop 1
	v_add_f32_dpp v0, v0, v0 row_mirror row_mask:0xf bank_mask:0xf bound_ctrl:1
	v_mov_b32_e32 v118, v0
	s_nop 1
	v_permlane16_swap_b32_e32 v0, v118
	v_add_f32_e32 v0, v0, v118
	v_mov_b32_e32 v118, v0
	s_nop 1
	v_permlane32_swap_b32_e32 v0, v118
	s_and_saveexec_b64 s[30:31], vcc
	v_add_f32_e32 v0, v0, v118
	v_fmamk_f32 v0, v0, 0x3a800000, v190
	v_mul_f32_e32 v118, 0x4b800000, v0
	v_cmp_gt_f32_e64 s[40:41], s96, v0
	s_lshl_b64 s[16:17], s[26:27], 2
	s_add_u32 s16, s6, s16
	v_cndmask_b32_e64 v0, v0, v118, s[40:41]
	v_rsq_f32_e32 v0, v0
	s_addc_u32 s17, s14, s17
	v_mul_f32_e32 v118, 0x45800000, v0
	v_cndmask_b32_e64 v0, v0, v118, s[40:41]
	global_store_dword v1, v0, s[16:17]
	s_or_b64 exec, exec, s[30:31]
	s_lshl_b64 s[16:17], s[26:27], 11
	v_cvt_pk_bf16_f32 v38, v38, v39
	v_cvt_pk_bf16_f32 v39, v40, v41
	v_cvt_pk_bf16_f32 v42, v42, v43
	v_cvt_pk_bf16_f32 v43, v44, v45
	v_cvt_pk_bf16_f32 v46, v46, v47
	v_cvt_pk_bf16_f32 v47, v48, v49
	v_cvt_pk_bf16_f32 v50, v50, v51
	v_cvt_pk_bf16_f32 v51, v52, v53
	v_lshl_add_u64 v[120:121], v[36:37], 0, s[16:17]
	global_store_dwordx2 v[120:121], v[38:39], off
	global_store_dwordx2 v[120:121], v[42:43], off offset:512
	global_store_dwordx2 v[120:121], v[46:47], off offset:1024
	global_store_dwordx2 v[120:121], v[50:51], off offset:1536
	s_add_i32 s26, s26, s88
	s_waitcnt vmcnt(31)
	v_mul_f32_e32 v0, v54, v54
	v_mul_f32_e32 v118, v55, v55
	v_mul_f32_e32 v119, v56, v56
	v_mul_f32_e32 v120, v57, v57
	v_fmac_f32_e32 v0, v58, v58
	v_fmac_f32_e32 v118, v59, v59
	v_fmac_f32_e32 v119, v60, v60
	v_fmac_f32_e32 v120, v61, v61
	v_fmac_f32_e32 v0, v62, v62
	v_fmac_f32_e32 v118, v63, v63
	v_fmac_f32_e32 v119, v64, v64
	v_fmac_f32_e32 v120, v65, v65
	v_fmac_f32_e32 v0, v66, v66
	v_fmac_f32_e32 v118, v67, v67
	v_fmac_f32_e32 v119, v68, v68
	v_fmac_f32_e32 v120, v69, v69
	v_add_f32_e32 v0, v0, v118
	v_add_f32_e32 v119, v119, v120
	v_add_f32_e32 v0, v0, v119
	s_nop 1
	v_add_f32_dpp v0, v0, v0 quad_perm:[1,0,3,2] row_mask:0xf bank_mask:0xf bound_ctrl:1
	s_nop 1
	v_add_f32_dpp v0, v0, v0 quad_perm:[2,3,0,1] row_mask:0xf bank_mask:0xf bound_ctrl:1
	s_nop 1
	v_add_f32_dpp v0, v0, v0 row_half_mirror row_mask:0xf bank_mask:0xf bound_ctrl:1
	s_nop 1
	v_add_f32_dpp v0, v0, v0 row_mirror row_mask:0xf bank_mask:0xf bound_ctrl:1
	v_mov_b32_e32 v118, v0
	s_nop 1
	v_permlane16_swap_b32_e32 v0, v118
	v_add_f32_e32 v0, v0, v118
	v_mov_b32_e32 v118, v0
	s_nop 1
	v_permlane32_swap_b32_e32 v0, v118
	s_and_saveexec_b64 s[30:31], vcc
	v_add_f32_e32 v0, v0, v118
	v_fmamk_f32 v0, v0, 0x3a800000, v190
	v_mul_f32_e32 v118, 0x4b800000, v0
	v_cmp_gt_f32_e64 s[40:41], s96, v0
	s_lshl_b64 s[16:17], s[26:27], 2
	s_add_u32 s16, s6, s16
	v_cndmask_b32_e64 v0, v0, v118, s[40:41]
	v_rsq_f32_e32 v0, v0
	s_addc_u32 s17, s14, s17
	v_mul_f32_e32 v118, 0x45800000, v0
	v_cndmask_b32_e64 v0, v0, v118, s[40:41]
	global_store_dword v1, v0, s[16:17]
	s_or_b64 exec, exec, s[30:31]
	s_lshl_b64 s[16:17], s[26:27], 11
	v_cvt_pk_bf16_f32 v54, v54, v55
	v_cvt_pk_bf16_f32 v55, v56, v57
	v_cvt_pk_bf16_f32 v58, v58, v59
	v_cvt_pk_bf16_f32 v59, v60, v61
	v_cvt_pk_bf16_f32 v62, v62, v63
	v_cvt_pk_bf16_f32 v63, v64, v65
	v_cvt_pk_bf16_f32 v66, v66, v67
	v_cvt_pk_bf16_f32 v67, v68, v69
	v_lshl_add_u64 v[120:121], v[36:37], 0, s[16:17]
	global_store_dwordx2 v[120:121], v[54:55], off
	global_store_dwordx2 v[120:121], v[58:59], off offset:512
	global_store_dwordx2 v[120:121], v[62:63], off offset:1024
	global_store_dwordx2 v[120:121], v[66:67], off offset:1536
	s_add_i32 s26, s26, s88
	s_waitcnt vmcnt(32)
	v_mul_f32_e32 v0, v70, v70
	v_mul_f32_e32 v118, v71, v71
	v_mul_f32_e32 v119, v72, v72
	v_mul_f32_e32 v120, v73, v73
	v_fmac_f32_e32 v0, v74, v74
	v_fmac_f32_e32 v118, v75, v75
	v_fmac_f32_e32 v119, v76, v76
	v_fmac_f32_e32 v120, v77, v77
	v_fmac_f32_e32 v0, v78, v78
	v_fmac_f32_e32 v118, v79, v79
	v_fmac_f32_e32 v119, v80, v80
	v_fmac_f32_e32 v120, v81, v81
	v_fmac_f32_e32 v0, v82, v82
	v_fmac_f32_e32 v118, v83, v83
	v_fmac_f32_e32 v119, v84, v84
	v_fmac_f32_e32 v120, v85, v85
	v_add_f32_e32 v0, v0, v118
	v_add_f32_e32 v119, v119, v120
	v_add_f32_e32 v0, v0, v119
	s_nop 1
	v_add_f32_dpp v0, v0, v0 quad_perm:[1,0,3,2] row_mask:0xf bank_mask:0xf bound_ctrl:1
	s_nop 1
	v_add_f32_dpp v0, v0, v0 quad_perm:[2,3,0,1] row_mask:0xf bank_mask:0xf bound_ctrl:1
	s_nop 1
	v_add_f32_dpp v0, v0, v0 row_half_mirror row_mask:0xf bank_mask:0xf bound_ctrl:1
	s_nop 1
	v_add_f32_dpp v0, v0, v0 row_mirror row_mask:0xf bank_mask:0xf bound_ctrl:1
	v_mov_b32_e32 v118, v0
	s_nop 1
	v_permlane16_swap_b32_e32 v0, v118
	v_add_f32_e32 v0, v0, v118
	v_mov_b32_e32 v118, v0
	s_nop 1
	v_permlane32_swap_b32_e32 v0, v118
	s_and_saveexec_b64 s[30:31], vcc
	v_add_f32_e32 v0, v0, v118
	v_fmamk_f32 v0, v0, 0x3a800000, v190
	v_mul_f32_e32 v118, 0x4b800000, v0
	v_cmp_gt_f32_e64 s[40:41], s96, v0
	s_lshl_b64 s[16:17], s[26:27], 2
	s_add_u32 s16, s6, s16
	v_cndmask_b32_e64 v0, v0, v118, s[40:41]
	v_rsq_f32_e32 v0, v0
	s_addc_u32 s17, s14, s17
	v_mul_f32_e32 v118, 0x45800000, v0
	v_cndmask_b32_e64 v0, v0, v118, s[40:41]
	global_store_dword v1, v0, s[16:17]
	s_or_b64 exec, exec, s[30:31]
	s_lshl_b64 s[16:17], s[26:27], 11
	v_cvt_pk_bf16_f32 v70, v70, v71
	v_cvt_pk_bf16_f32 v71, v72, v73
	v_cvt_pk_bf16_f32 v74, v74, v75
	v_cvt_pk_bf16_f32 v75, v76, v77
	v_cvt_pk_bf16_f32 v78, v78, v79
	v_cvt_pk_bf16_f32 v79, v80, v81
	v_cvt_pk_bf16_f32 v82, v82, v83
	v_cvt_pk_bf16_f32 v83, v84, v85
	v_lshl_add_u64 v[120:121], v[36:37], 0, s[16:17]
	global_store_dwordx2 v[120:121], v[70:71], off
	global_store_dwordx2 v[120:121], v[74:75], off offset:512
	global_store_dwordx2 v[120:121], v[78:79], off offset:1024
	global_store_dwordx2 v[120:121], v[82:83], off offset:1536
	s_add_i32 s26, s26, s88
	s_waitcnt vmcnt(33)
	v_mul_f32_e32 v0, v86, v86
	v_mul_f32_e32 v118, v87, v87
	v_mul_f32_e32 v119, v88, v88
	v_mul_f32_e32 v120, v89, v89
	v_fmac_f32_e32 v0, v90, v90
	v_fmac_f32_e32 v118, v91, v91
	v_fmac_f32_e32 v119, v92, v92
	v_fmac_f32_e32 v120, v93, v93
	v_fmac_f32_e32 v0, v94, v94
	v_fmac_f32_e32 v118, v95, v95
	v_fmac_f32_e32 v119, v96, v96
	v_fmac_f32_e32 v120, v97, v97
	v_fmac_f32_e32 v0, v98, v98
	v_fmac_f32_e32 v118, v99, v99
	v_fmac_f32_e32 v119, v100, v100
	v_fmac_f32_e32 v120, v101, v101
	v_add_f32_e32 v0, v0, v118
	v_add_f32_e32 v119, v119, v120
	v_add_f32_e32 v0, v0, v119
	s_nop 1
	v_add_f32_dpp v0, v0, v0 quad_perm:[1,0,3,2] row_mask:0xf bank_mask:0xf bound_ctrl:1
	s_nop 1
	v_add_f32_dpp v0, v0, v0 quad_perm:[2,3,0,1] row_mask:0xf bank_mask:0xf bound_ctrl:1
	s_nop 1
	v_add_f32_dpp v0, v0, v0 row_half_mirror row_mask:0xf bank_mask:0xf bound_ctrl:1
	s_nop 1
	v_add_f32_dpp v0, v0, v0 row_mirror row_mask:0xf bank_mask:0xf bound_ctrl:1
	v_mov_b32_e32 v118, v0
	s_nop 1
	v_permlane16_swap_b32_e32 v0, v118
	v_add_f32_e32 v0, v0, v118
	v_mov_b32_e32 v118, v0
	s_nop 1
	v_permlane32_swap_b32_e32 v0, v118
	s_and_saveexec_b64 s[30:31], vcc
	v_add_f32_e32 v0, v0, v118
	v_fmamk_f32 v0, v0, 0x3a800000, v190
	v_mul_f32_e32 v118, 0x4b800000, v0
	v_cmp_gt_f32_e64 s[40:41], s96, v0
	s_lshl_b64 s[16:17], s[26:27], 2
	s_add_u32 s16, s6, s16
	v_cndmask_b32_e64 v0, v0, v118, s[40:41]
	v_rsq_f32_e32 v0, v0
	s_addc_u32 s17, s14, s17
	v_mul_f32_e32 v118, 0x45800000, v0
	v_cndmask_b32_e64 v0, v0, v118, s[40:41]
	global_store_dword v1, v0, s[16:17]
	s_or_b64 exec, exec, s[30:31]
	s_lshl_b64 s[16:17], s[26:27], 11
	v_cvt_pk_bf16_f32 v86, v86, v87
	v_cvt_pk_bf16_f32 v87, v88, v89
	v_cvt_pk_bf16_f32 v90, v90, v91
	v_cvt_pk_bf16_f32 v91, v92, v93
	v_cvt_pk_bf16_f32 v94, v94, v95
	v_cvt_pk_bf16_f32 v95, v96, v97
	v_cvt_pk_bf16_f32 v98, v98, v99
	v_cvt_pk_bf16_f32 v99, v100, v101
	v_lshl_add_u64 v[120:121], v[36:37], 0, s[16:17]
	global_store_dwordx2 v[120:121], v[86:87], off
	global_store_dwordx2 v[120:121], v[90:91], off offset:512
	global_store_dwordx2 v[120:121], v[94:95], off offset:1024
	global_store_dwordx2 v[120:121], v[98:99], off offset:1536
	s_add_i32 s26, s26, s88
	s_waitcnt vmcnt(34)
	v_mul_f32_e32 v0, v102, v102
	v_mul_f32_e32 v118, v103, v103
	v_mul_f32_e32 v119, v104, v104
	v_mul_f32_e32 v120, v105, v105
	v_fmac_f32_e32 v0, v106, v106
	v_fmac_f32_e32 v118, v107, v107
	v_fmac_f32_e32 v119, v108, v108
	v_fmac_f32_e32 v120, v109, v109
	v_fmac_f32_e32 v0, v110, v110
	v_fmac_f32_e32 v118, v111, v111
	v_fmac_f32_e32 v119, v112, v112
	v_fmac_f32_e32 v120, v113, v113
	v_fmac_f32_e32 v0, v114, v114
	v_fmac_f32_e32 v118, v115, v115
	v_fmac_f32_e32 v119, v116, v116
	v_fmac_f32_e32 v120, v117, v117
	v_add_f32_e32 v0, v0, v118
	v_add_f32_e32 v119, v119, v120
	v_add_f32_e32 v0, v0, v119
	s_nop 1
	v_add_f32_dpp v0, v0, v0 quad_perm:[1,0,3,2] row_mask:0xf bank_mask:0xf bound_ctrl:1
	s_nop 1
	v_add_f32_dpp v0, v0, v0 quad_perm:[2,3,0,1] row_mask:0xf bank_mask:0xf bound_ctrl:1
	s_nop 1
	v_add_f32_dpp v0, v0, v0 row_half_mirror row_mask:0xf bank_mask:0xf bound_ctrl:1
	s_nop 1
	v_add_f32_dpp v0, v0, v0 row_mirror row_mask:0xf bank_mask:0xf bound_ctrl:1
	v_mov_b32_e32 v118, v0
	s_nop 1
	v_permlane16_swap_b32_e32 v0, v118
	v_add_f32_e32 v0, v0, v118
	v_mov_b32_e32 v118, v0
	s_nop 1
	v_permlane32_swap_b32_e32 v0, v118
	s_and_saveexec_b64 s[30:31], vcc
	v_add_f32_e32 v0, v0, v118
	v_fmamk_f32 v0, v0, 0x3a800000, v190
	v_mul_f32_e32 v118, 0x4b800000, v0
	v_cmp_gt_f32_e64 s[40:41], s96, v0
	s_lshl_b64 s[16:17], s[26:27], 2
	s_add_u32 s16, s6, s16
	v_cndmask_b32_e64 v0, v0, v118, s[40:41]
	v_rsq_f32_e32 v0, v0
	s_addc_u32 s17, s14, s17
	v_mul_f32_e32 v118, 0x45800000, v0
	v_cndmask_b32_e64 v0, v0, v118, s[40:41]
	global_store_dword v1, v0, s[16:17]
	s_or_b64 exec, exec, s[30:31]
	s_lshl_b64 s[16:17], s[26:27], 11
	v_cvt_pk_bf16_f32 v102, v102, v103
	v_cvt_pk_bf16_f32 v103, v104, v105
	v_cvt_pk_bf16_f32 v106, v106, v107
	v_cvt_pk_bf16_f32 v107, v108, v109
	v_cvt_pk_bf16_f32 v110, v110, v111
	v_cvt_pk_bf16_f32 v111, v112, v113
	v_cvt_pk_bf16_f32 v114, v114, v115
	v_cvt_pk_bf16_f32 v115, v116, v117
	v_lshl_add_u64 v[120:121], v[36:37], 0, s[16:17]
	global_store_dwordx2 v[120:121], v[102:103], off
	global_store_dwordx2 v[120:121], v[106:107], off offset:512
	global_store_dwordx2 v[120:121], v[110:111], off offset:1024
	global_store_dwordx2 v[120:121], v[114:115], off offset:1536
	s_add_i32 s26, s26, s88
	s_waitcnt vmcnt(30)
	v_mul_f32_e32 v0, v2, v2
	v_mul_f32_e32 v118, v3, v3
	v_mul_f32_e32 v119, v4, v4
	v_mul_f32_e32 v120, v5, v5
	v_fmac_f32_e32 v0, v6, v6
	v_fmac_f32_e32 v118, v7, v7
	v_fmac_f32_e32 v119, v8, v8
	v_fmac_f32_e32 v120, v9, v9
	v_fmac_f32_e32 v0, v10, v10
	v_fmac_f32_e32 v118, v11, v11
	v_fmac_f32_e32 v119, v12, v12
	v_fmac_f32_e32 v120, v13, v13
	v_fmac_f32_e32 v0, v14, v14
	v_fmac_f32_e32 v118, v15, v15
	v_fmac_f32_e32 v119, v16, v16
	v_fmac_f32_e32 v120, v17, v17
	v_add_f32_e32 v0, v0, v118
	v_add_f32_e32 v119, v119, v120
	v_add_f32_e32 v0, v0, v119
	s_nop 1
	v_add_f32_dpp v0, v0, v0 quad_perm:[1,0,3,2] row_mask:0xf bank_mask:0xf bound_ctrl:1
	s_nop 1
	v_add_f32_dpp v0, v0, v0 quad_perm:[2,3,0,1] row_mask:0xf bank_mask:0xf bound_ctrl:1
	s_nop 1
	v_add_f32_dpp v0, v0, v0 row_half_mirror row_mask:0xf bank_mask:0xf bound_ctrl:1
	s_nop 1
	v_add_f32_dpp v0, v0, v0 row_mirror row_mask:0xf bank_mask:0xf bound_ctrl:1
	v_mov_b32_e32 v118, v0
	s_nop 1
	v_permlane16_swap_b32_e32 v0, v118
	v_add_f32_e32 v0, v0, v118
	v_mov_b32_e32 v118, v0
	s_nop 1
	v_permlane32_swap_b32_e32 v0, v118
	s_and_saveexec_b64 s[30:31], vcc
	v_add_f32_e32 v0, v0, v118
	v_fmamk_f32 v0, v0, 0x3a800000, v190
	v_mul_f32_e32 v118, 0x4b800000, v0
	v_cmp_gt_f32_e64 s[40:41], s96, v0
	s_lshl_b64 s[16:17], s[26:27], 2
	s_add_u32 s16, s6, s16
	v_cndmask_b32_e64 v0, v0, v118, s[40:41]
	v_rsq_f32_e32 v0, v0
	s_addc_u32 s17, s14, s17
	v_mul_f32_e32 v118, 0x45800000, v0
	v_cndmask_b32_e64 v0, v0, v118, s[40:41]
	global_store_dword v1, v0, s[16:17]
	s_or_b64 exec, exec, s[30:31]
	s_lshl_b64 s[16:17], s[26:27], 11
	v_cvt_pk_bf16_f32 v2, v2, v3
	v_cvt_pk_bf16_f32 v3, v4, v5
	v_cvt_pk_bf16_f32 v6, v6, v7
	v_cvt_pk_bf16_f32 v7, v8, v9
	v_cvt_pk_bf16_f32 v10, v10, v11
	v_cvt_pk_bf16_f32 v11, v12, v13
	v_cvt_pk_bf16_f32 v14, v14, v15
	v_cvt_pk_bf16_f32 v15, v16, v17
	v_lshl_add_u64 v[120:121], v[36:37], 0, s[16:17]
	global_store_dwordx2 v[120:121], v[2:3], off
	global_store_dwordx2 v[120:121], v[6:7], off offset:512
	global_store_dwordx2 v[120:121], v[10:11], off offset:1024
	global_store_dwordx2 v[120:121], v[14:15], off offset:1536
	s_add_i32 s26, s26, s88
	s_mov_b32 s4, s26
	s_cmpk_gt_i32 s4, 0x3fff
	s_cbranch_scc1 .LBB0_1062
	s_branch .LBB0_1055
